# speedup vs baseline: 1.0300x; 1.0300x over previous
_Z11edge_kernelILi36ELb1EEvPKfS1_PKDF16_PKiS5_S1_S1_S1_S1_S1_PDF16_:
	s_load_dwordx4 s[4:7], s[0:1], 0x38
	s_load_dwordx2 s[8:9], s[0:1], 0x28
	s_load_dwordx2 s[10:11], s[0:1], 0x48
	v_lshlrev_b32_e32 v136, 4, v0
	v_mov_b32_e32 v137, 0
	v_readfirstlane_b32 s3, v0
	s_lshl_b32 s2, s2, 1
	s_waitcnt lgkmcnt(0)
	v_lshl_add_u64 v[2:3], s[10:11], 0, v[136:137]
	global_load_dwordx4 v[28:31], v136, s[10:11]
	global_load_dwordx4 v[70:73], v136, s[10:11] offset:2048
	s_movk_i32 s10, 0x1000
	v_add_co_u32_e32 v4, vcc, s10, v2
	s_movk_i32 s10, 0x2000
	s_nop 0
	v_addc_co_u32_e32 v5, vcc, 0, v3, vcc
	s_lshr_b32 s16, s3, 6
	v_add_co_u32_e32 v6, vcc, s10, v2
	s_add_i32 s2, s16, s2
	v_lshrrev_b32_e32 v1, 4, v0
	v_addc_co_u32_e32 v7, vcc, 0, v3, vcc
	s_movk_i32 s10, 0x3000
	s_ashr_i32 s3, s2, 31
	s_mul_i32 s11, s2, 0x2400
	v_and_b32_e32 v78, 3, v1
	v_add_co_u32_e32 v2, vcc, s10, v2
	s_mul_hi_i32 s10, s2, 0x2400
	s_add_u32 s8, s8, s11
	v_and_b32_e32 v79, 15, v0
	s_addc_u32 s9, s9, s10
	v_mul_u32_u24_e32 v0, 0x90, v78
	v_mov_b32_e32 v1, v137
	v_lshl_add_u64 v[0:1], v[0:1], 4, s[8:9]
	s_lshl_b64 s[8:9], s[2:3], 14
	v_addc_co_u32_e32 v3, vcc, 0, v3, vcc
	s_add_u32 s4, s4, s8
	global_load_dwordx4 v[74:77], v[6:7], off offset:-4096
	global_load_dwordx4 v[80:83], v[6:7], off
	global_load_dwordx4 v[84:87], v[6:7], off offset:2048
	global_load_dwordx4 v[88:91], v[4:5], off offset:2048
	global_load_dwordx4 v[92:95], v[2:3], off
	global_load_dwordx4 v[96:99], v[2:3], off offset:2048
	v_lshlrev_b32_e32 v68, 4, v79
	v_mov_b32_e32 v69, v137
	s_addc_u32 s5, s5, s9
	v_lshlrev_b32_e32 v2, 12, v78
	v_mov_b32_e32 v3, v137
	v_lshl_add_u64 v[0:1], v[0:1], 0, v[68:69]
	v_lshl_add_u64 v[2:3], s[4:5], 0, v[2:3]
	global_load_dwordx4 v[100:103], v[0:1], off nt
	global_load_dwordx4 v[104:107], v[0:1], off offset:256 nt
	global_load_dwordx4 v[108:111], v[0:1], off offset:512 nt
	global_load_dwordx4 v[112:115], v[0:1], off offset:768 nt
	global_load_dwordx4 v[116:119], v[0:1], off offset:1024 nt
	global_load_dwordx4 v[120:123], v[0:1], off offset:1280 nt
	global_load_dwordx4 v[124:127], v[0:1], off offset:1536 nt
	global_load_dwordx4 v[128:131], v[0:1], off offset:1792 nt
	global_load_dwordx4 v[132:135], v[0:1], off offset:2048 nt
	v_lshl_add_u64 v[0:1], v[2:3], 0, v[68:69]
	global_load_dwordx4 v[60:63], v[0:1], off nt
	global_load_dwordx4 v[64:67], v[0:1], off offset:256 nt
	global_load_dwordx4 v[56:59], v[0:1], off offset:512 nt
	global_load_dwordx4 v[52:55], v[0:1], off offset:768 nt
	global_load_dwordx4 v[44:47], v[0:1], off offset:1024 nt
	global_load_dwordx4 v[48:51], v[0:1], off offset:1280 nt
	global_load_dwordx4 v[40:43], v[0:1], off offset:1536 nt
	global_load_dwordx4 v[36:39], v[0:1], off offset:1792 nt
	global_load_dwordx4 v[24:27], v[0:1], off offset:2048 nt
	global_load_dwordx4 v[32:35], v[0:1], off offset:2304 nt
	global_load_dwordx4 v[20:23], v[0:1], off offset:2560 nt
	global_load_dwordx4 v[16:19], v[0:1], off offset:2816 nt
	global_load_dwordx4 v[8:11], v[0:1], off offset:3072 nt
	global_load_dwordx4 v[12:15], v[0:1], off offset:3328 nt
	global_load_dwordx4 v[4:7], v[0:1], off offset:3584 nt
	s_nop 0
	global_load_dwordx4 v[0:3], v[0:1], off offset:3840 nt
	s_load_dwordx4 s[8:11], s[0:1], 0x0
	s_load_dwordx4 s[12:15], s[0:1], 0x18
	s_load_dwordx2 s[18:19], s[0:1], 0x30
	v_mul_u32_u24_e32 v69, 9, v78
	s_lshl_b64 s[4:5], s[2:3], 2
	s_waitcnt lgkmcnt(0)
	s_add_u32 s12, s12, s4
	s_waitcnt vmcnt(32)
	ds_write_b128 v136, v[28:31]
	s_waitcnt vmcnt(31)
	ds_write_b128 v136, v[70:73] offset:2048
	s_waitcnt vmcnt(30)
	ds_write_b128 v136, v[74:77] offset:4096
	s_waitcnt vmcnt(27)
	ds_write_b128 v136, v[88:91] offset:6144
	s_addc_u32 s13, s13, s5
	s_load_dword s12, s[12:13], 0x0
	ds_write_b128 v136, v[80:83] offset:8192
	ds_write_b128 v136, v[84:87] offset:10240
	s_waitcnt vmcnt(26)
	ds_write_b128 v136, v[92:95] offset:12288
	s_waitcnt vmcnt(25)
	ds_write_b128 v136, v[96:99] offset:14336
	v_lshlrev_b32_e32 v136, 2, v69
	v_cmp_eq_u32_e32 vcc, 3, v78
	v_mbcnt_lo_u32_b32 v69, -1, 0
	s_waitcnt lgkmcnt(0)
	s_ashr_i32 s13, s12, 31
	s_add_u32 s4, s14, s4
	s_addc_u32 s5, s15, s5
	s_lshl_b64 s[14:15], s[2:3], 8
	s_add_u32 s18, s18, s14
	s_addc_u32 s19, s19, s15
	s_add_u32 s6, s6, s14
	s_addc_u32 s7, s7, s15
	s_lshl_b64 s[14:15], s[12:13], 4
	s_add_u32 s10, s10, s14
	s_addc_u32 s11, s11, s15
	s_lshl_b64 s[12:13], s[12:13], 7
	s_add_u32 s8, s8, s12
	s_addc_u32 s9, s9, s13
	global_load_dwordx4 v[70:73], v136, s[8:9] nt
	v_lshl_add_u64 v[30:31], s[10:11], 0, v[136:137]
	s_movk_i32 s10, 0xff94
	v_lshl_add_u64 v[28:29], s[8:9], 0, v[136:137]
	s_mov_b32 s11, -1
	v_lshl_add_u64 v[28:29], v[28:29], 0, 20
	v_lshl_add_u64 v[30:31], v[30:31], 0, s[10:11]
	v_cndmask_b32_e32 v81, v29, v31, vcc
	v_cndmask_b32_e32 v80, v28, v30, vcc
	global_load_dwordx4 v[74:77], v[80:81], off nt
	global_load_dword v82, v136, s[8:9] offset:16 nt
	global_load_dwordx4 v[96:99], v68, s[18:19] nt
	global_load_dwordx4 v[28:31], v68, s[6:7] nt
	v_mbcnt_hi_u32_b32 v69, -1, v69
	v_xor_b32_e32 v83, 32, v69
	v_and_b32_e32 v81, 64, v69
	v_xor_b32_e32 v80, 16, v69
	v_add_u32_e32 v81, 64, v81
	v_cmp_lt_i32_e32 vcc, v80, v81
	s_load_dword s4, s[4:5], 0x0
	s_lshl_b32 s5, s16, 8
	v_cndmask_b32_e32 v80, v69, v80, vcc
	v_lshlrev_b32_e32 v80, 2, v80
	v_cmp_lt_i32_e32 vcc, v83, v81
	s_waitcnt lgkmcnt(0)
	s_barrier
	v_cndmask_b32_e32 v69, v69, v83, vcc
	v_lshlrev_b32_e32 v69, 2, v69
	s_addk_i32 s5, 0x4000
	v_cmp_eq_u32_e32 vcc, 0, v78
	v_lshl_add_u32 v81, v79, 4, s5
	s_waitcnt vmcnt(4)
	v_pk_fma_f32 v[84:85], v[70:71], v[102:103], 0 op_sel_hi:[0,1,0]
	v_pk_fma_f32 v[86:87], v[70:71], v[100:101], 0 op_sel_hi:[0,1,0]
	v_pk_fma_f32 v[86:87], v[70:71], v[104:105], v[86:87] op_sel:[1,0,0]
	v_pk_fma_f32 v[70:71], v[70:71], v[106:107], v[84:85] op_sel:[1,0,0]
	v_mov_b32_e32 v88, v73
	v_pk_fma_f32 v[70:71], v[72:73], v[110:111], v[70:71] op_sel_hi:[0,1,1]
	v_pk_fma_f32 v[72:73], v[72:73], v[108:109], v[86:87] op_sel_hi:[0,1,1]
	v_pk_fma_f32 v[72:73], v[88:89], v[112:113], v[72:73] op_sel_hi:[0,1,1]
	v_pk_fma_f32 v[70:71], v[88:89], v[114:115], v[70:71] op_sel_hi:[0,1,1]
	s_waitcnt vmcnt(2)
	v_pk_fma_f32 v[70:71], v[82:83], v[118:119], v[70:71] op_sel_hi:[0,1,1]
	v_pk_fma_f32 v[72:73], v[82:83], v[116:117], v[72:73] op_sel_hi:[0,1,1]
	v_pk_fma_f32 v[72:73], v[74:75], v[120:121], v[72:73] op_sel_hi:[0,1,1]
	v_pk_fma_f32 v[70:71], v[74:75], v[122:123], v[70:71] op_sel_hi:[0,1,1]
	v_pk_fma_f32 v[70:71], v[74:75], v[126:127], v[70:71] op_sel:[1,0,0]
	v_pk_fma_f32 v[72:73], v[74:75], v[124:125], v[72:73] op_sel:[1,0,0]
	v_mov_b32_e32 v84, v77
	v_pk_fma_f32 v[72:73], v[76:77], v[128:129], v[72:73] op_sel_hi:[0,1,1]
	v_pk_fma_f32 v[70:71], v[76:77], v[130:131], v[70:71] op_sel_hi:[0,1,1]
	v_pk_fma_f32 v[74:75], v[84:85], v[134:135], v[70:71] op_sel_hi:[0,1,1]
	v_pk_fma_f32 v[70:71], v[84:85], v[132:133], v[72:73] op_sel_hi:[0,1,1]
	ds_bpermute_b32 v72, v80, v70
	ds_bpermute_b32 v73, v80, v71
	ds_bpermute_b32 v76, v80, v74
	ds_bpermute_b32 v77, v80, v75
	s_waitcnt lgkmcnt(2)
	v_pk_add_f32 v[70:71], v[70:71], v[72:73]
	s_waitcnt lgkmcnt(0)
	v_pk_add_f32 v[72:73], v[74:75], v[76:77]
	ds_bpermute_b32 v76, v69, v70
	ds_bpermute_b32 v77, v69, v71
	ds_bpermute_b32 v74, v69, v72
	ds_bpermute_b32 v75, v69, v73
	s_and_saveexec_b64 s[6:7], vcc
	s_cbranch_execz .LBB2_2
	s_waitcnt lgkmcnt(0)
	v_pk_add_f32 v[70:71], v[70:71], v[76:77]
	v_pk_add_f32 v[72:73], v[72:73], v[74:75]
	s_waitcnt vmcnt(1)
	v_pk_add_f32 v[72:73], v[98:99], v[72:73]
	v_pk_add_f32 v[70:71], v[96:97], v[70:71]
	v_max_f32_e32 v72, 0, v72
	v_max_f32_e32 v70, 0, v70
	v_max_f32_e32 v71, 0, v71
	v_max_f32_e32 v73, 0, v73
	ds_write_b128 v81, v[70:73]

_Z11edge_kernelILi64ELb0EEvPKfS1_PKDF16_PKiS5_S1_S1_S1_S1_S1_PDF16_:
	s_load_dwordx8 s[4:11], s[0:1], 0x10
	s_load_dwordx4 s[12:15], s[0:1], 0x38
	s_load_dwordx2 s[16:17], s[0:1], 0x48
	s_load_dwordx2 s[20:21], s[0:1], 0x30
	v_lshlrev_b32_e32 v164, 4, v0
	v_mov_b32_e32 v165, 0
	v_readfirstlane_b32 s3, v0
	s_lshl_b32 s2, s2, 1
	s_waitcnt lgkmcnt(0)
	v_lshl_add_u64 v[2:3], s[16:17], 0, v[164:165]
	global_load_dwordx4 v[128:131], v164, s[16:17]
	global_load_dwordx4 v[136:139], v164, s[16:17] offset:2048
	s_movk_i32 s16, 0x1000
	v_add_co_u32_e32 v4, vcc, s16, v2
	s_movk_i32 s16, 0x2000
	s_nop 0
	v_addc_co_u32_e32 v5, vcc, 0, v3, vcc
	v_add_co_u32_e32 v6, vcc, s16, v2
	s_movk_i32 s16, 0x3000
	s_nop 0
	v_addc_co_u32_e32 v7, vcc, 0, v3, vcc
	v_add_co_u32_e32 v2, vcc, s16, v2
	s_lshr_b32 s16, s3, 6
	s_add_i32 s2, s16, s2
	s_ashr_i32 s3, s2, 31
	s_lshl_b64 s[18:19], s[2:3], 14
	v_bfe_u32 v134, v0, 4, 2
	s_add_u32 s10, s10, s18
	v_addc_co_u32_e32 v3, vcc, 0, v3, vcc
	v_and_b32_e32 v135, 15, v0
	s_addc_u32 s11, s11, s19
	v_lshlrev_b32_e32 v0, 12, v134
	v_mov_b32_e32 v1, v165
	global_load_dwordx4 v[140:143], v[6:7], off offset:-4096
	global_load_dwordx4 v[144:147], v[6:7], off
	global_load_dwordx4 v[148:151], v[6:7], off offset:2048
	global_load_dwordx4 v[152:155], v[4:5], off offset:2048
	global_load_dwordx4 v[156:159], v[2:3], off
	global_load_dwordx4 v[160:163], v[2:3], off offset:2048
	v_lshl_add_u64 v[2:3], s[10:11], 0, v[0:1]
	s_add_u32 s10, s12, s18
	s_addc_u32 s11, s13, s19
	v_lshlrev_b32_e32 v132, 4, v135
	v_mov_b32_e32 v133, v165
	v_lshl_add_u64 v[0:1], s[10:11], 0, v[0:1]
	v_lshl_add_u64 v[2:3], v[2:3], 0, v[132:133]
	v_lshl_add_u64 v[0:1], v[0:1], 0, v[132:133]
	global_load_dwordx4 v[124:127], v[2:3], off nt
	global_load_dwordx4 v[120:123], v[2:3], off offset:256 nt
	global_load_dwordx4 v[116:119], v[2:3], off offset:512 nt
	global_load_dwordx4 v[112:115], v[2:3], off offset:768 nt
	global_load_dwordx4 v[108:111], v[2:3], off offset:1024 nt
	global_load_dwordx4 v[104:107], v[2:3], off offset:1280 nt
	global_load_dwordx4 v[100:103], v[2:3], off offset:1536 nt
	global_load_dwordx4 v[96:99], v[2:3], off offset:1792 nt
	global_load_dwordx4 v[92:95], v[2:3], off offset:2048 nt
	global_load_dwordx4 v[88:91], v[2:3], off offset:2304 nt
	global_load_dwordx4 v[84:87], v[2:3], off offset:2560 nt
	global_load_dwordx4 v[80:83], v[2:3], off offset:2816 nt
	global_load_dwordx4 v[76:79], v[2:3], off offset:3072 nt
	global_load_dwordx4 v[72:75], v[2:3], off offset:3328 nt
	global_load_dwordx4 v[68:71], v[2:3], off offset:3584 nt
	global_load_dwordx4 v[64:67], v[2:3], off offset:3840 nt
	global_load_dwordx4 v[56:59], v[0:1], off nt
	global_load_dwordx4 v[60:63], v[0:1], off offset:256 nt
	global_load_dwordx4 v[52:55], v[0:1], off offset:512 nt
	global_load_dwordx4 v[48:51], v[0:1], off offset:768 nt
	global_load_dwordx4 v[40:43], v[0:1], off offset:1024 nt
	global_load_dwordx4 v[44:47], v[0:1], off offset:1280 nt
	global_load_dwordx4 v[36:39], v[0:1], off offset:1536 nt
	global_load_dwordx4 v[32:35], v[0:1], off offset:1792 nt
	global_load_dwordx4 v[24:27], v[0:1], off offset:2048 nt
	global_load_dwordx4 v[28:31], v[0:1], off offset:2304 nt
	global_load_dwordx4 v[20:23], v[0:1], off offset:2560 nt
	global_load_dwordx4 v[16:19], v[0:1], off offset:2816 nt
	global_load_dwordx4 v[8:11], v[0:1], off offset:3072 nt
	global_load_dwordx4 v[12:15], v[0:1], off offset:3328 nt
	global_load_dwordx4 v[4:7], v[0:1], off offset:3584 nt
	s_nop 0
	global_load_dwordx4 v[0:3], v[0:1], off offset:3840 nt
	s_lshl_b64 s[10:11], s[2:3], 2
	s_add_u32 s6, s6, s10
	s_waitcnt vmcnt(39)
	ds_write_b128 v164, v[128:131]
	s_waitcnt vmcnt(38)
	ds_write_b128 v164, v[136:139] offset:2048
	s_waitcnt vmcnt(37)
	ds_write_b128 v164, v[140:143] offset:4096
	s_addc_u32 s7, s7, s11
	s_load_dword s12, s[6:7], 0x0
	v_lshlrev_b32_e32 v128, 5, v134
	s_waitcnt vmcnt(36)
	ds_write_b128 v164, v[144:147] offset:8192
	s_waitcnt vmcnt(34)
	ds_write_b128 v164, v[152:155] offset:6144
	s_waitcnt lgkmcnt(0)
	s_ashr_i32 s13, s12, 31
	s_add_u32 s6, s8, s10
	s_addc_u32 s7, s9, s11
	s_lshl_b64 s[8:9], s[2:3], 8
	s_add_u32 s20, s20, s8
	s_addc_u32 s21, s21, s9
	s_add_u32 s8, s14, s8
	s_addc_u32 s9, s15, s9
	s_lshl_b64 s[10:11], s[12:13], 7
	s_add_u32 s4, s4, s10
	s_addc_u32 s5, s5, s11
	global_load_dwordx4 v[138:141], v128, s[4:5] nt
	global_load_dwordx4 v[142:145], v128, s[4:5] offset:16 nt
	v_mbcnt_lo_u32_b32 v128, -1, 0
	v_mbcnt_hi_u32_b32 v128, -1, v128
	v_and_b32_e32 v130, 64, v128
	v_xor_b32_e32 v129, 16, v128
	v_add_u32_e32 v130, 64, v130
	v_xor_b32_e32 v131, 32, v128
	v_cmp_lt_i32_e32 vcc, v129, v130
	ds_write_b128 v164, v[148:151] offset:10240
	s_waitcnt vmcnt(35)
	ds_write_b128 v164, v[156:159] offset:12288
	s_waitcnt vmcnt(34)
	ds_write_b128 v164, v[160:163] offset:14336
	v_cndmask_b32_e32 v129, v128, v129, vcc
	v_cmp_lt_i32_e32 vcc, v131, v130
	v_lshlrev_b32_e32 v136, 2, v129
	s_load_dword s4, s[6:7], 0x0
	v_cndmask_b32_e32 v128, v128, v131, vcc
	v_lshlrev_b32_e32 v133, 2, v128
	global_load_dwordx4 v[156:159], v132, s[20:21] nt
	global_load_dwordx4 v[128:131], v132, s[8:9] nt
	s_lshl_b32 s5, s16, 8
	s_waitcnt lgkmcnt(0)
	s_barrier
	s_addk_i32 s5, 0x4000
	v_cmp_eq_u32_e32 vcc, 0, v134
	s_waitcnt vmcnt(3)
	v_cvt_f32_f16_e32 v137, v138
	v_cvt_f32_f16_sdwa v146, v138 dst_sel:DWORD dst_unused:UNUSED_PAD src0_sel:WORD_1
	v_cvt_f32_f16_e32 v147, v139
	v_cvt_f32_f16_sdwa v139, v139 dst_sel:DWORD dst_unused:UNUSED_PAD src0_sel:WORD_1
	v_cvt_f32_f16_e32 v150, v141
	v_cvt_f32_f16_sdwa v141, v141 dst_sel:DWORD dst_unused:UNUSED_PAD src0_sel:WORD_1
	v_cvt_f32_f16_e32 v148, v140
	s_waitcnt vmcnt(2)
	v_cvt_f32_f16_e32 v153, v143
	v_max_f32_e32 v138, 0, v137
	v_cvt_f32_f16_sdwa v137, v143 dst_sel:DWORD dst_unused:UNUSED_PAD src0_sel:WORD_1
	v_cvt_f32_f16_e32 v143, v144
	v_cvt_f32_f16_sdwa v149, v140 dst_sel:DWORD dst_unused:UNUSED_PAD src0_sel:WORD_1
	v_pk_fma_f32 v[126:127], v[138:139], v[126:127], 0 op_sel_hi:[0,1,0]
	v_pk_fma_f32 v[124:125], v[138:139], v[124:125], 0 op_sel_hi:[0,1,0]
	v_max_f32_e32 v138, 0, v146
	v_max_f32_e32 v140, 0, v147
	v_pk_fma_f32 v[122:123], v[138:139], v[122:123], v[126:127] op_sel_hi:[0,1,1]
	v_pk_fma_f32 v[120:121], v[138:139], v[120:121], v[124:125] op_sel_hi:[0,1,1]
	v_cvt_f32_f16_e32 v151, v142
	v_cvt_f32_f16_sdwa v152, v142 dst_sel:DWORD dst_unused:UNUSED_PAD src0_sel:WORD_1
	v_max_f32_e32 v142, 0, v139
	v_pk_fma_f32 v[116:117], v[140:141], v[116:117], v[120:121] op_sel_hi:[0,1,1]
	v_pk_fma_f32 v[118:119], v[140:141], v[118:119], v[122:123] op_sel_hi:[0,1,1]
	v_cvt_f32_f16_e32 v155, v145
	v_cvt_f32_f16_sdwa v145, v145 dst_sel:DWORD dst_unused:UNUSED_PAD src0_sel:WORD_1
	v_max_f32_e32 v124, 0, v148
	v_pk_fma_f32 v[114:115], v[142:143], v[114:115], v[118:119] op_sel_hi:[0,1,1]
	v_pk_fma_f32 v[112:113], v[142:143], v[112:113], v[116:117] op_sel_hi:[0,1,1]
	v_max_f32_e32 v126, 0, v149
	v_pk_fma_f32 v[108:109], v[124:125], v[108:109], v[112:113] op_sel_hi:[0,1,1]
	v_pk_fma_f32 v[110:111], v[124:125], v[110:111], v[114:115] op_sel_hi:[0,1,1]
	v_max_f32_e32 v138, 0, v150
	v_pk_fma_f32 v[106:107], v[126:127], v[106:107], v[110:111] op_sel_hi:[0,1,1]
	v_pk_fma_f32 v[104:105], v[126:127], v[104:105], v[108:109] op_sel_hi:[0,1,1]
	v_cvt_f32_f16_sdwa v154, v144 dst_sel:DWORD dst_unused:UNUSED_PAD src0_sel:WORD_1
	v_max_f32_e32 v144, 0, v141
	v_pk_fma_f32 v[100:101], v[138:139], v[100:101], v[104:105] op_sel_hi:[0,1,1]
	v_pk_fma_f32 v[102:103], v[138:139], v[102:103], v[106:107] op_sel_hi:[0,1,1]
	v_max_f32_e32 v146, 0, v151
	v_pk_fma_f32 v[98:99], v[144:145], v[98:99], v[102:103] op_sel_hi:[0,1,1]
	v_pk_fma_f32 v[96:97], v[144:145], v[96:97], v[100:101] op_sel_hi:[0,1,1]
	v_max_f32_e32 v148, 0, v152
	v_pk_fma_f32 v[92:93], v[146:147], v[92:93], v[96:97] op_sel_hi:[0,1,1]
	v_pk_fma_f32 v[94:95], v[146:147], v[94:95], v[98:99] op_sel_hi:[0,1,1]
	v_max_f32_e32 v120, 0, v153
	v_pk_fma_f32 v[90:91], v[148:149], v[90:91], v[94:95] op_sel_hi:[0,1,1]
	v_pk_fma_f32 v[88:89], v[148:149], v[88:89], v[92:93] op_sel_hi:[0,1,1]
	v_max_f32_e32 v122, 0, v137
	v_pk_fma_f32 v[84:85], v[120:121], v[84:85], v[88:89] op_sel_hi:[0,1,1]
	v_pk_fma_f32 v[86:87], v[120:121], v[86:87], v[90:91] op_sel_hi:[0,1,1]
	v_max_f32_e32 v140, 0, v143
	v_pk_fma_f32 v[82:83], v[122:123], v[82:83], v[86:87] op_sel_hi:[0,1,1]
	v_pk_fma_f32 v[80:81], v[122:123], v[80:81], v[84:85] op_sel_hi:[0,1,1]
	v_max_f32_e32 v150, 0, v154
	v_pk_fma_f32 v[76:77], v[140:141], v[76:77], v[80:81] op_sel_hi:[0,1,1]
	v_pk_fma_f32 v[78:79], v[140:141], v[78:79], v[82:83] op_sel_hi:[0,1,1]
	v_max_f32_e32 v152, 0, v155
	v_pk_fma_f32 v[74:75], v[150:151], v[74:75], v[78:79] op_sel_hi:[0,1,1]
	v_pk_fma_f32 v[72:73], v[150:151], v[72:73], v[76:77] op_sel_hi:[0,1,1]
	v_max_f32_e32 v154, 0, v145
	v_pk_fma_f32 v[68:69], v[152:153], v[68:69], v[72:73] op_sel_hi:[0,1,1]
	v_pk_fma_f32 v[70:71], v[152:153], v[70:71], v[74:75] op_sel_hi:[0,1,1]
	v_pk_fma_f32 v[66:67], v[154:155], v[66:67], v[70:71] op_sel_hi:[0,1,1]
	v_pk_fma_f32 v[64:65], v[154:155], v[64:65], v[68:69] op_sel_hi:[0,1,1]
	ds_bpermute_b32 v68, v136, v64
	ds_bpermute_b32 v69, v136, v65
	ds_bpermute_b32 v70, v136, v66
	ds_bpermute_b32 v71, v136, v67
	v_lshl_add_u32 v72, v135, 4, s5
	s_waitcnt lgkmcnt(2)
	v_pk_add_f32 v[64:65], v[64:65], v[68:69]
	s_waitcnt lgkmcnt(0)
	v_pk_add_f32 v[66:67], v[66:67], v[70:71]
	ds_bpermute_b32 v70, v133, v64
	ds_bpermute_b32 v71, v133, v65
	ds_bpermute_b32 v68, v133, v66
	ds_bpermute_b32 v69, v133, v67
	s_and_saveexec_b64 s[6:7], vcc
	s_cbranch_execz .LBB3_2
	s_waitcnt lgkmcnt(0)
	v_pk_add_f32 v[64:65], v[64:65], v[70:71]
	v_pk_add_f32 v[66:67], v[66:67], v[68:69]
	s_waitcnt vmcnt(1)
	v_pk_add_f32 v[66:67], v[158:159], v[66:67]
	v_pk_add_f32 v[64:65], v[156:157], v[64:65]
	v_max_f32_e32 v66, 0, v66
	v_max_f32_e32 v64, 0, v64
	v_max_f32_e32 v65, 0, v65
	v_max_f32_e32 v67, 0, v67
	ds_write_b128 v72, v[64:67]
